# early combine pass lightly throttled (one s_sleep per row) on top of nt streaming
# speedup vs baseline: 1.0082x; 1.0082x over previous
; __device__ __forceinline__ float bf_lo(unsigned w) { return __uint_as_float(w << 16); }
; __device__ __forceinline__ float bf_hi(unsigned w) { return __uint_as_float(w & 0xffff0000u); }
; __device__ __forceinline__ f32x4 ld4_bf(const bf16_t* p) { const u32x2 w = *(const u32x2*)p; return (f32x4){bf_lo(w.x), bf_hi(w.x), bf_lo(w.y), bf_hi(w.y)}; }
; __device__ __forceinline__ float sq4(const f32x4 v) { return (v[0] * v[0] + v[1] * v[1]) + (v[2] * v[2] + v[3] * v[3]); }
; __device__ __forceinline__ void phase_final(const Ctx& P, volatile LAS int* tab, int vcu, int G) {
;     ...
;     for (int row = gw; row < ML; row += NGW) {
;         const int e1 = tok[row * 8], pos1 = tok[row * 8 + 1], e2 = tok[row * 8 + 2], pos2 = tok[row * 8 + 3]; const float p1 = ((const float*)tok)[row * 8 + 4], p2 = ((const float*)tok)[row * 8 + 5];
;         const bf16_t* y1 = YB + (size_t)(tab[8 + e1] * 256 + pos1) * DM; const bf16_t* y2 = YB + (size_t)(tab[8 + e2] * 256 + pos2) * DM;
;         const bf16_t* xr = (const bf16_t*)(P.ws + WS_XA) + (size_t)row * DM; const float* g2 = mod + (size_t)(row >> 12) * NMOD + 5 * DM;
;         f32x4 v[8]; float ss = 0.f;
; #pragma unroll
;         for (int j = 0; j < 8; ++j) { const int c = 4 * lane + 256 * j; const f32x4 x4 = ld4_bf(xr + c), g4 = *(const f32x4*)(g2 + c); const u32x2 a = *(const u32x2*)(y1 + c), b = *(const u32x2*)(y2 + c);
;             const f32x4 ya = (f32x4){bf_lo(a.x), bf_hi(a.x), bf_lo(a.y), bf_hi(a.y)}, yb = (f32x4){bf_lo(b.x), bf_hi(b.x), bf_lo(b.y), bf_hi(b.y)};
;             v[j] = x4 + g4 * (ya * p1 + yb * p2); ss += sq4(v[j]); }
.LBB0_2712:
	v_mov_b32_e32 v16, v194
	v_mov_b32_e32 v17, v195
	v_mov_b32_e32 v18, v196
	v_mov_b32_e32 v19, v197
	v_mov_b32_e32 v46, v198
	v_mov_b32_e32 v47, v199
	v_max_i32_e32 v200, v194, v196
	s_ashr_i32 s3, s10, 12
	s_mul_hi_i32 s8, s3, 0xc000
	s_mul_i32 s3, s3, 0xc000
	s_add_u32 s3, s36, s3
	s_addc_u32 s9, s37, s8
	s_add_u32 s8, s3, 0x146000
	s_addc_u32 s9, s9, 0
	s_add_i32 s10, s10, s0
	s_add_i32 s2, s2, s13
	s_ashr_i32 s3, s2, 31
	s_lshl_b64 s[14:15], s[2:3], 2
	s_add_u32 s14, s11, s14
	s_addc_u32 s15, s12, s15
	s_cmpk_lt_i32 s10, 0x4000
	s_cselect_b32 s17, 1, 0
	v_readfirstlane_b32 s16, v200
	s_cmp_lt_i32 s16, s20
	s_cbranch_scc1 .Lp16_skip
	s_cmp_ge_i32 s16, s21
	s_cbranch_scc1 .Lp16_skip
	v_lshlrev_b32_e32 v0, 2, v16
	v_lshlrev_b32_e32 v1, 2, v18
	v_add_u32_e32 v0, s1, v0
	v_add_u32_e32 v1, s1, v1
	ds_read_b32 v16, v0 offset:32
	ds_read_b32 v18, v1 offset:32
	global_load_dwordx2 v[48:49], v[34:35], off offset:-2048 nt
	global_load_dwordx2 v[50:51], v[34:35], off offset:-1536 nt
	global_load_dwordx2 v[52:53], v[34:35], off offset:-1024 nt
	global_load_dwordx4 v[0:3], v28, s[8:9]
	global_load_dwordx2 v[54:55], v[34:35], off offset:-512 nt
	global_load_dwordx4 v[8:11], v64, s[8:9]
	global_load_dwordx4 v[4:7], v65, s[8:9]
	global_load_dwordx4 v[12:15], v66, s[8:9]
	global_load_dwordx2 v[56:57], v[34:35], off nt
	global_load_dwordx4 v[20:23], v36, s[8:9]
	global_load_dwordx4 v[24:27], v38, s[8:9]
	global_load_dwordx2 v[76:77], v[34:35], off offset:512 nt
	global_load_dwordx2 v[78:79], v[34:35], off offset:1024 nt
	global_load_dwordx2 v[80:81], v[34:35], off offset:1536 nt
	global_load_dwordx4 v[68:71], v40, s[8:9]
	global_load_dwordx4 v[72:75], v42, s[8:9]
	v_lshl_add_u64 v[34:35], v[34:35], 0, s[6:7]
	s_waitcnt lgkmcnt(0)
	v_lshlrev_b32_e32 v16, 8, v16
	v_lshlrev_b32_e32 v18, 8, v18
	v_add_u32_e32 v16, v16, v17
	v_add_u32_e32 v18, v18, v19
	v_ashrrev_i32_e32 v17, 31, v16
	v_ashrrev_i32_e32 v19, 31, v18
	v_lshlrev_b64 v[16:17], 12, v[16:17]
	v_lshlrev_b64 v[18:19], 12, v[18:19]
	v_lshl_add_u64 v[16:17], v[30:31], 0, v[16:17]
	v_lshl_add_u64 v[18:19], v[30:31], 0, v[18:19]
	global_load_dwordx2 v[84:85], v[16:17], off nt
	global_load_dwordx2 v[86:87], v[18:19], off nt
	global_load_dwordx2 v[88:89], v[16:17], off offset:512 nt
	global_load_dwordx2 v[90:91], v[18:19], off offset:512 nt
	global_load_dwordx2 v[92:93], v[16:17], off offset:1024 nt
	global_load_dwordx2 v[94:95], v[18:19], off offset:1024 nt
	global_load_dwordx2 v[96:97], v[16:17], off offset:1536 nt
	global_load_dwordx2 v[98:99], v[18:19], off offset:1536 nt
	global_load_dwordx2 v[100:101], v[16:17], off offset:2048 nt
	global_load_dwordx2 v[102:103], v[18:19], off offset:2048 nt
	global_load_dwordx2 v[104:105], v[16:17], off offset:2560 nt
	global_load_dwordx2 v[106:107], v[16:17], off offset:3072 nt
	global_load_dwordx2 v[108:109], v[16:17], off offset:3584 nt
	global_load_dwordx2 v[110:111], v[18:19], off offset:2560 nt
	global_load_dwordx2 v[112:113], v[18:19], off offset:3072 nt
	global_load_dwordx2 v[114:115], v[18:19], off offset:3584 nt
	global_load_dwordx4 v[194:197], v29, s[14:15]
	global_load_dwordx2 v[198:199], v29, s[14:15] offset:16
	s_waitcnt vmcnt(2)
	v_lshlrev_b32_e32 v116, 16, v48
	v_and_b32_e32 v117, 0xffff0000, v48
	v_lshlrev_b32_e32 v48, 16, v49
	v_and_b32_e32 v49, 0xffff0000, v49
	v_lshlrev_b32_e32 v118, 16, v50
	v_and_b32_e32 v119, 0xffff0000, v50
	v_lshlrev_b32_e32 v50, 16, v51
	v_and_b32_e32 v51, 0xffff0000, v51
	v_lshlrev_b32_e32 v120, 16, v52
	v_and_b32_e32 v121, 0xffff0000, v52
	v_lshlrev_b32_e32 v52, 16, v53
	v_and_b32_e32 v53, 0xffff0000, v53
	v_lshlrev_b32_e32 v124, 16, v56
	v_and_b32_e32 v125, 0xffff0000, v56
	v_lshlrev_b32_e32 v132, 16, v86
	v_and_b32_e32 v133, 0xffff0000, v86
	v_lshlrev_b32_e32 v86, 16, v87
	v_and_b32_e32 v87, 0xffff0000, v87
	v_lshlrev_b32_e32 v136, 16, v90
	v_and_b32_e32 v137, 0xffff0000, v90
	v_lshlrev_b32_e32 v90, 16, v91
	v_and_b32_e32 v91, 0xffff0000, v91
	v_lshlrev_b32_e32 v82, 16, v84
	v_and_b32_e32 v83, 0xffff0000, v84
	v_lshlrev_b32_e32 v84, 16, v85
	v_and_b32_e32 v85, 0xffff0000, v85
	v_lshlrev_b32_e32 v134, 16, v88
	v_and_b32_e32 v135, 0xffff0000, v88
	v_lshlrev_b32_e32 v88, 16, v89
	v_and_b32_e32 v89, 0xffff0000, v89
	v_lshlrev_b32_e32 v140, 16, v94
	v_and_b32_e32 v141, 0xffff0000, v94
	v_lshlrev_b32_e32 v94, 16, v95
	v_and_b32_e32 v95, 0xffff0000, v95
	v_lshlrev_b32_e32 v148, 16, v102
	v_and_b32_e32 v149, 0xffff0000, v102
	v_lshlrev_b32_e32 v102, 16, v103
	v_and_b32_e32 v103, 0xffff0000, v103
	v_lshlrev_b32_e32 v156, 16, v112
	v_and_b32_e32 v157, 0xffff0000, v112
	v_lshlrev_b32_e32 v112, 16, v113
	v_and_b32_e32 v113, 0xffff0000, v113
	v_pk_mul_f32 v[86:87], v[46:47], v[86:87] op_sel:[1,0]
	v_pk_mul_f32 v[132:133], v[46:47], v[132:133] op_sel:[1,0]
	v_pk_mul_f32 v[90:91], v[46:47], v[90:91] op_sel:[1,0]
	v_pk_mul_f32 v[136:137], v[46:47], v[136:137] op_sel:[1,0]
	v_lshlrev_b32_e32 v138, 16, v92
	v_and_b32_e32 v139, 0xffff0000, v92
	v_lshlrev_b32_e32 v92, 16, v93
	v_and_b32_e32 v93, 0xffff0000, v93
	v_lshlrev_b32_e32 v144, 16, v98
	v_and_b32_e32 v145, 0xffff0000, v98
	v_lshlrev_b32_e32 v98, 16, v99
	v_and_b32_e32 v99, 0xffff0000, v99
	v_lshlrev_b32_e32 v146, 16, v100
	v_and_b32_e32 v147, 0xffff0000, v100
	v_lshlrev_b32_e32 v100, 16, v101
	v_and_b32_e32 v101, 0xffff0000, v101
	v_lshlrev_b32_e32 v152, 16, v110
	v_and_b32_e32 v153, 0xffff0000, v110
	v_lshlrev_b32_e32 v110, 16, v111
	v_and_b32_e32 v111, 0xffff0000, v111
	v_lshlrev_b32_e32 v154, 16, v106
	v_and_b32_e32 v155, 0xffff0000, v106
	v_lshlrev_b32_e32 v106, 16, v107
	v_and_b32_e32 v107, 0xffff0000, v107
	v_lshlrev_b32_e32 v160, 16, v114
; __device__ __forceinline__ float bf_lo(unsigned w) { return __uint_as_float(w << 16); }
; __device__ __forceinline__ float bf_hi(unsigned w) { return __uint_as_float(w & 0xffff0000u); }
; __device__ __forceinline__ f32x4 ld4_bf(const bf16_t* p) { const u32x2 w = *(const u32x2*)p; return (f32x4){bf_lo(w.x), bf_hi(w.x), bf_lo(w.y), bf_hi(w.y)}; }
; __device__ __forceinline__ float sq4(const f32x4 v) { return (v[0] * v[0] + v[1] * v[1]) + (v[2] * v[2] + v[3] * v[3]); }
; __device__ __forceinline__ void phase_final(const Ctx& P, volatile LAS int* tab, int vcu, int G) {
;     ...
;         for (int j = 0; j < 8; ++j) { const int c = 4 * lane + 256 * j; const f32x4 x4 = ld4_bf(xr + c), g4 = *(const f32x4*)(g2 + c); const u32x2 a = *(const u32x2*)(y1 + c), b = *(const u32x2*)(y2 + c);
;             const f32x4 ya = (f32x4){bf_lo(a.x), bf_hi(a.x), bf_lo(a.y), bf_hi(a.y)}, yb = (f32x4){bf_lo(b.x), bf_hi(b.x), bf_lo(b.y), bf_hi(b.y)};
;             v[j] = x4 + g4 * (ya * p1 + yb * p2); ss += sq4(v[j]); }
;         ss = wave_sum(ss); const float rstd = __builtin_amdgcn_rsqf(ss * (1.0f / DM) + EPS);
	v_and_b32_e32 v161, 0xffff0000, v114
	v_lshlrev_b32_e32 v114, 16, v115
	v_and_b32_e32 v115, 0xffff0000, v115
	v_pk_mul_f32 v[140:141], v[46:47], v[140:141] op_sel:[1,0]
	v_pk_mul_f32 v[94:95], v[46:47], v[94:95] op_sel:[1,0]
	v_pk_mul_f32 v[102:103], v[46:47], v[102:103] op_sel:[1,0]
	v_pk_mul_f32 v[112:113], v[46:47], v[112:113] op_sel:[1,0]
	v_pk_fma_f32 v[82:83], v[46:47], v[82:83], v[132:133] op_sel_hi:[0,1,1]
	v_pk_fma_f32 v[84:85], v[46:47], v[84:85], v[86:87] op_sel_hi:[0,1,1]
	v_pk_fma_f32 v[86:87], v[46:47], v[134:135], v[136:137] op_sel_hi:[0,1,1]
	v_pk_fma_f32 v[88:89], v[46:47], v[88:89], v[90:91] op_sel_hi:[0,1,1]
	v_lshlrev_b32_e32 v56, 16, v57
	v_and_b32_e32 v57, 0xffff0000, v57
	v_lshlrev_b32_e32 v128, 16, v78
	v_and_b32_e32 v129, 0xffff0000, v78
	v_lshlrev_b32_e32 v78, 16, v79
	v_and_b32_e32 v79, 0xffff0000, v79
	v_lshlrev_b32_e32 v142, 16, v96
	v_and_b32_e32 v143, 0xffff0000, v96
	v_lshlrev_b32_e32 v96, 16, v97
	v_and_b32_e32 v97, 0xffff0000, v97
	v_lshlrev_b32_e32 v150, 16, v104
	v_and_b32_e32 v151, 0xffff0000, v104
	v_lshlrev_b32_e32 v104, 16, v105
	v_and_b32_e32 v105, 0xffff0000, v105
	v_lshlrev_b32_e32 v158, 16, v108
	v_and_b32_e32 v159, 0xffff0000, v108
	v_lshlrev_b32_e32 v108, 16, v109
	v_and_b32_e32 v109, 0xffff0000, v109
	v_pk_mul_f32 v[98:99], v[46:47], v[98:99] op_sel:[1,0]
	v_pk_mul_f32 v[144:145], v[46:47], v[144:145] op_sel:[1,0]
	v_pk_mul_f32 v[148:149], v[46:47], v[148:149] op_sel:[1,0]
	v_pk_mul_f32 v[152:153], v[46:47], v[152:153] op_sel:[1,0]
	v_pk_mul_f32 v[110:111], v[46:47], v[110:111] op_sel:[1,0]
	v_pk_mul_f32 v[156:157], v[46:47], v[156:157] op_sel:[1,0]
	v_pk_mul_f32 v[114:115], v[46:47], v[114:115] op_sel:[1,0]
	v_pk_mul_f32 v[160:161], v[46:47], v[160:161] op_sel:[1,0]
	v_pk_fma_f32 v[90:91], v[46:47], v[92:93], v[94:95] op_sel_hi:[0,1,1]
	v_pk_fma_f32 v[92:93], v[46:47], v[138:139], v[140:141] op_sel_hi:[0,1,1]
	v_pk_fma_f32 v[100:101], v[46:47], v[100:101], v[102:103] op_sel_hi:[0,1,1]
	v_pk_fma_f32 v[106:107], v[46:47], v[106:107], v[112:113] op_sel_hi:[0,1,1]
	v_pk_fma_f32 v[2:3], v[2:3], v[84:85], v[48:49]
	v_pk_fma_f32 v[0:1], v[0:1], v[82:83], v[116:117]
	v_pk_fma_f32 v[10:11], v[10:11], v[88:89], v[50:51]
	v_pk_fma_f32 v[8:9], v[8:9], v[86:87], v[118:119]
	v_lshlrev_b32_e32 v122, 16, v54
	v_and_b32_e32 v123, 0xffff0000, v54
	v_lshlrev_b32_e32 v54, 16, v55
	v_and_b32_e32 v55, 0xffff0000, v55
	v_lshlrev_b32_e32 v130, 16, v80
	v_and_b32_e32 v131, 0xffff0000, v80
	v_lshlrev_b32_e32 v80, 16, v81
	v_and_b32_e32 v81, 0xffff0000, v81
	v_pk_fma_f32 v[94:95], v[46:47], v[142:143], v[144:145] op_sel_hi:[0,1,1]
	v_pk_fma_f32 v[96:97], v[46:47], v[96:97], v[98:99] op_sel_hi:[0,1,1]
	v_pk_fma_f32 v[98:99], v[46:47], v[146:147], v[148:149] op_sel_hi:[0,1,1]
	v_pk_fma_f32 v[102:103], v[46:47], v[104:105], v[110:111] op_sel_hi:[0,1,1]
	v_pk_fma_f32 v[104:105], v[46:47], v[150:151], v[152:153] op_sel_hi:[0,1,1]
	v_pk_fma_f32 v[110:111], v[46:47], v[154:155], v[156:157] op_sel_hi:[0,1,1]
	v_pk_fma_f32 v[112:113], v[46:47], v[158:159], v[160:161] op_sel_hi:[0,1,1]
	v_pk_fma_f32 v[46:47], v[46:47], v[108:109], v[114:115] op_sel_hi:[0,1,1]
	v_pk_fma_f32 v[4:5], v[4:5], v[92:93], v[120:121]
	v_pk_fma_f32 v[6:7], v[6:7], v[90:91], v[52:53]
	v_pk_fma_f32 v[22:23], v[22:23], v[100:101], v[56:57]
	v_pk_fma_f32 v[48:49], v[70:71], v[106:107], v[78:79]
	v_mov_b32_e32 v56, v1
	v_mov_b32_e32 v57, v9
	v_mov_b32_e32 v70, v3
	v_mov_b32_e32 v71, v11
	v_pk_fma_f32 v[14:15], v[14:15], v[96:97], v[54:55]
	v_pk_fma_f32 v[50:51], v[68:69], v[110:111], v[128:129]
	v_pk_fma_f32 v[46:47], v[74:75], v[46:47], v[80:81]
	v_pk_fma_f32 v[52:53], v[72:73], v[112:113], v[130:131]
	v_mov_b32_e32 v54, v0
	v_mov_b32_e32 v55, v8
	v_mov_b32_e32 v68, v2
	v_mov_b32_e32 v69, v10
	v_pk_mul_f32 v[72:73], v[6:7], v[6:7]
	v_pk_mul_f32 v[74:75], v[4:5], v[4:5]
	v_pk_mul_f32 v[56:57], v[56:57], v[56:57]
	v_pk_mul_f32 v[70:71], v[70:71], v[70:71]
	v_lshlrev_b32_e32 v126, 16, v76
	v_and_b32_e32 v127, 0xffff0000, v76
	v_lshlrev_b32_e32 v76, 16, v77
	v_and_b32_e32 v77, 0xffff0000, v77
	v_pk_fma_f32 v[12:13], v[12:13], v[94:95], v[122:123]
	v_pk_mov_b32 v[88:89], v[74:75], v[72:73] op_sel:[1,0]
	v_mov_b32_e32 v75, v73
	v_pk_fma_f32 v[54:55], v[54:55], v[54:55], v[56:57]
	v_pk_fma_f32 v[56:57], v[68:69], v[68:69], v[70:71]
	v_pk_fma_f32 v[20:21], v[20:21], v[98:99], v[124:125]
	v_pk_fma_f32 v[26:27], v[26:27], v[102:103], v[76:77]
	v_mul_f32_e32 v76, v13, v13
	v_mul_f32_e32 v78, v15, v15
	v_pk_add_f32 v[68:69], v[88:89], v[74:75]
	v_pk_add_f32 v[54:55], v[54:55], v[56:57]
	v_pk_fma_f32 v[24:25], v[24:25], v[104:105], v[126:127]
	v_mul_f32_e32 v87, v20, v20
	v_mul_f32_e32 v90, v21, v21
	v_mul_f32_e32 v91, v22, v22
	v_mul_f32_e32 v92, v23, v23
	v_pk_fma_f32 v[72:73], v[12:13], v[12:13], v[76:77] op_sel_hi:[1,1,0]
	v_pk_fma_f32 v[76:77], v[14:15], v[14:15], v[78:79] op_sel_hi:[1,1,0]
	v_pk_add_f32 v[56:57], v[68:69], v[68:69] op_sel:[0,1] op_sel_hi:[1,0]
	v_pk_add_f32 v[54:55], v[54:55], v[54:55] op_sel:[0,1] op_sel_hi:[1,0]
	v_pk_mul_f32 v[80:81], v[26:27], v[26:27]
	v_pk_mul_f32 v[82:83], v[24:25], v[24:25]
	v_mov_b32_e32 v73, v91
	v_mov_b32_e32 v77, v92
	v_mov_b32_e32 v57, v90
	v_mov_b32_e32 v55, v87
	v_pk_mov_b32 v[78:79], v[82:83], v[80:81] op_sel:[1,0]
	v_mov_b32_e32 v83, v81
	v_pk_add_f32 v[68:69], v[72:73], v[76:77]
	v_pk_add_f32 v[54:55], v[54:55], v[56:57]
	v_mul_f32_e32 v84, v51, v51
	v_mul_f32_e32 v86, v49, v49
	v_pk_add_f32 v[70:71], v[78:79], v[82:83]
	v_pk_add_f32 v[54:55], v[54:55], v[68:69]
	v_mul_f32_e32 v93, v52, v52
	v_mul_f32_e32 v94, v53, v53
	v_mul_f32_e32 v95, v46, v46
	v_mul_f32_e32 v96, v47, v47
	v_pk_fma_f32 v[80:81], v[50:51], v[50:51], v[84:85] op_sel_hi:[1,1,0]
	v_pk_fma_f32 v[84:85], v[48:49], v[48:49], v[86:87] op_sel_hi:[1,1,0]
	v_pk_add_f32 v[70:71], v[70:71], v[70:71] op_sel:[0,1] op_sel_hi:[1,0]
	v_pk_add_f32 v[54:55], v[54:55], v[54:55] op_sel:[0,1] op_sel_hi:[1,0]
	v_mov_b32_e32 v81, v95
	v_mov_b32_e32 v85, v96
	v_mov_b32_e32 v71, v94
	v_mov_b32_e32 v55, v93
	v_pk_add_f32 v[72:73], v[80:81], v[84:85]
	v_pk_add_f32 v[54:55], v[54:55], v[70:71]
	s_nop 0
	v_pk_add_f32 v[54:55], v[54:55], v[72:73]
	s_nop 0
	v_add_f32_e32 v54, v54, v55
	ds_bpermute_b32 v55, v58, v54
	s_waitcnt lgkmcnt(0)
; __device__ __forceinline__ void phase_final(const Ctx& P, volatile LAS int* tab, int vcu, int G) {
;     ...
;         ss = wave_sum(ss); const float rstd = __builtin_amdgcn_rsqf(ss * (1.0f / DM) + EPS);
; #pragma unroll
;         for (int j = 0; j < 8; ++j) { const int c = 4 * lane + 256 * j; const f32x4 fg = *(const f32x4*)(P.in[34] + c); *(f32x4*)(P.out + (size_t)row * DM + c) = v[j] * rstd * fg; }
	v_add_f32_e32 v54, v54, v55
	ds_bpermute_b32 v55, v59, v54
	s_waitcnt lgkmcnt(0)
	v_add_f32_e32 v54, v54, v55
	ds_bpermute_b32 v55, v60, v54
	s_waitcnt lgkmcnt(0)
	v_add_f32_e32 v54, v54, v55
	ds_bpermute_b32 v55, v61, v54
	s_waitcnt lgkmcnt(0)
	v_add_f32_e32 v54, v54, v55
	ds_bpermute_b32 v55, v62, v54
	s_waitcnt lgkmcnt(0)
	v_add_f32_e32 v54, v54, v55
	ds_bpermute_b32 v55, v63, v54
	s_waitcnt lgkmcnt(0)
	v_add_f32_e32 v54, v54, v55
	v_fmamk_f32 v54, v54, 0x3a000000, v67
	v_rsq_f32_e32 v54, v54
	s_nop 0
	v_pk_mul_f32 v[0:1], v[0:1], v[54:55] op_sel_hi:[1,0]
	v_pk_mul_f32 v[2:3], v[2:3], v[54:55] op_sel_hi:[1,0]
	v_pk_mul_f32 v[8:9], v[8:9], v[54:55] op_sel_hi:[1,0]
	v_pk_mul_f32 v[10:11], v[10:11], v[54:55] op_sel_hi:[1,0]
	v_pk_mul_f32 v[4:5], v[4:5], v[54:55] op_sel_hi:[1,0]
	v_pk_mul_f32 v[6:7], v[6:7], v[54:55] op_sel_hi:[1,0]
	v_pk_mul_f32 v[12:13], v[12:13], v[54:55] op_sel_hi:[1,0]
	v_pk_mul_f32 v[14:15], v[14:15], v[54:55] op_sel_hi:[1,0]
	v_pk_mul_f32 v[20:21], v[20:21], v[54:55] op_sel_hi:[1,0]
	v_pk_mul_f32 v[22:23], v[22:23], v[54:55] op_sel_hi:[1,0]
	v_pk_mul_f32 v[24:25], v[24:25], v[54:55] op_sel_hi:[1,0]
	v_pk_mul_f32 v[26:27], v[26:27], v[54:55] op_sel_hi:[1,0]
	v_pk_mul_f32 v[68:69], v[50:51], v[54:55] op_sel_hi:[1,0]
	v_pk_mul_f32 v[70:71], v[48:49], v[54:55] op_sel_hi:[1,0]
	v_pk_mul_f32 v[72:73], v[52:53], v[54:55] op_sel_hi:[1,0]
	v_pk_mul_f32 v[74:75], v[46:47], v[54:55] op_sel_hi:[1,0]
	v_pk_mul_f32 v[0:1], v[162:163], v[0:1]
	v_pk_mul_f32 v[2:3], v[164:165], v[2:3]
	global_store_dwordx4 v[32:33], v[0:3], off offset:-4096 nt
	v_pk_mul_f32 v[8:9], v[166:167], v[8:9]
	v_pk_mul_f32 v[10:11], v[168:169], v[10:11]
	global_store_dwordx4 v[32:33], v[8:11], off offset:-3072 nt
	v_pk_mul_f32 v[4:5], v[170:171], v[4:5]
	v_pk_mul_f32 v[6:7], v[172:173], v[6:7]
	global_store_dwordx4 v[32:33], v[4:7], off offset:-2048 nt
	v_pk_mul_f32 v[12:13], v[174:175], v[12:13]
	v_pk_mul_f32 v[14:15], v[176:177], v[14:15]
	global_store_dwordx4 v[32:33], v[12:15], off offset:-1024 nt
	v_pk_mul_f32 v[20:21], v[178:179], v[20:21]
	v_pk_mul_f32 v[22:23], v[180:181], v[22:23]
	global_store_dwordx4 v[32:33], v[20:23], off nt
	v_pk_mul_f32 v[24:25], v[182:183], v[24:25]
	v_pk_mul_f32 v[26:27], v[184:185], v[26:27]
	global_store_dwordx4 v[32:33], v[24:27], off offset:1024 nt
	v_pk_mul_f32 v[68:69], v[186:187], v[68:69]
	v_pk_mul_f32 v[70:71], v[188:189], v[70:71]
	global_store_dwordx4 v[32:33], v[68:71], off offset:2048 nt
	v_pk_mul_f32 v[72:73], v[190:191], v[72:73]
	v_pk_mul_f32 v[74:75], v[192:193], v[74:75]
	global_store_dwordx4 v[32:33], v[72:75], off offset:3072 nt
	v_lshl_add_u64 v[32:33], v[32:33], 0, s[4:5]
	s_waitcnt vmcnt(8)
	s_cmp_eq_u32 s99, 2
	s_cbranch_scc0 .Lp16_nosleep
	s_sleep 127
